# MoE expert-table setup in P14/P15: the 8 expert-count loads issued together instead of 8 dependent round trips
# speedup vs baseline: 1.0069x; 1.0069x over previous
; #define LAS __attribute__((address_space(3)))
; __device__ __forceinline__ int tid_opaque() { int t = threadIdx.x; asm volatile("" : "+v"(t)); return t; }
; __device__ __forceinline__ void moe_tables(const Ctx& P, volatile LAS int* tab, int nN) {
;     if (tid_opaque() == 0) { const unsigned* ecnt = (const unsigned*)(P.ws + WS_CTL) + CW_ECNT; int pb = 0, cu = 0;
;         for (int e = 0; e < 8; ++e) { const int c = (int)ecnt[64 * e], np = (c + 255) >> 8; tab[e] = c; tab[8 + e] = pb; tab[16 + e] = cu; pb += np; cu += np * nN; }
;         tab[24] = cu; }
;     __syncthreads();
; }
.LBB0_2524:
	s_or_b64 exec, exec, s[40:41]
	s_mov_b64 s[2:3], s[0:1]
	s_nop 0
	v_mov_b64_e32 v[2:3], s[2:3]
	flat_load_dword v1, v[2:3] offset:296
	s_waitcnt vmcnt(0) lgkmcnt(0)
	v_cmp_gt_i32_e32 vcc, 15, v1
	s_and_saveexec_b64 s[10:11], vcc
	s_cbranch_execz .LBB0_2557
	s_mov_b64 s[2:3], s[0:1]
	s_nop 0
	v_mov_b64_e32 v[2:3], s[2:3]
	flat_load_dword v1, v[2:3] offset:300
	s_waitcnt vmcnt(0) lgkmcnt(0)
	v_cmp_lt_i32_e32 vcc, 14, v1
	s_and_b64 exec, exec, vcc
	s_cbranch_execz .LBB0_2557
	s_mov_b64 s[2:3], s[0:1]
	s_mov_b64 s[2:3], s[0:1]
	v_mov_b32_e32 v1, v0
	s_nop 0
	v_cmp_eq_u32_e32 vcc, 0, v1
	s_and_saveexec_b64 s[2:3], vcc
	s_cbranch_execz .LBB0_2528
	v_mov_b32_e32 v1, 0x4000
	global_load_dword v2, v1, s[36:37]
	global_load_dword v3, v1, s[36:37] offset:256
	global_load_dword v4, v1, s[36:37] offset:512
	global_load_dword v5, v1, s[36:37] offset:768
	global_load_dword v6, v1, s[36:37] offset:1024
	global_load_dword v7, v1, s[36:37] offset:1280
	global_load_dword v8, v1, s[36:37] offset:1536
	global_load_dword v9, v1, s[36:37] offset:1792
	v_mov_b32_e32 v10, 0x20100
	v_mov_b32_e32 v11, 0
	v_mov_b32_e32 v13, 0
	s_waitcnt vmcnt(0)
	ds_write_b32 v10, v2
	ds_write_b32 v10, v11 offset:32
	ds_write_b32 v10, v13 offset:64
	v_add_u32_e32 v12, 0xff, v2
	v_ashrrev_i32_e32 v12, 8, v12
	v_add_u32_e32 v11, v11, v12
	v_mul_u32_u24_e32 v13, 56, v11
	ds_write_b32 v10, v3 offset:4
	ds_write_b32 v10, v11 offset:36
	ds_write_b32 v10, v13 offset:68
	v_add_u32_e32 v12, 0xff, v3
	v_ashrrev_i32_e32 v12, 8, v12
	v_add_u32_e32 v11, v11, v12
	v_mul_u32_u24_e32 v13, 56, v11
	ds_write_b32 v10, v4 offset:8
	ds_write_b32 v10, v11 offset:40
	ds_write_b32 v10, v13 offset:72
	v_add_u32_e32 v12, 0xff, v4
	v_ashrrev_i32_e32 v12, 8, v12
	v_add_u32_e32 v11, v11, v12
	v_mul_u32_u24_e32 v13, 56, v11
	ds_write_b32 v10, v5 offset:12
	ds_write_b32 v10, v11 offset:44
	ds_write_b32 v10, v13 offset:76
	v_add_u32_e32 v12, 0xff, v5
	v_ashrrev_i32_e32 v12, 8, v12
	v_add_u32_e32 v11, v11, v12
	v_mul_u32_u24_e32 v13, 56, v11
	ds_write_b32 v10, v6 offset:16
	ds_write_b32 v10, v11 offset:48
	ds_write_b32 v10, v13 offset:80
	v_add_u32_e32 v12, 0xff, v6
	v_ashrrev_i32_e32 v12, 8, v12
	v_add_u32_e32 v11, v11, v12
	v_mul_u32_u24_e32 v13, 56, v11
	ds_write_b32 v10, v7 offset:20
	ds_write_b32 v10, v11 offset:52
	ds_write_b32 v10, v13 offset:84
	v_add_u32_e32 v12, 0xff, v7
	v_ashrrev_i32_e32 v12, 8, v12
	v_add_u32_e32 v11, v11, v12
	v_mul_u32_u24_e32 v13, 56, v11
	ds_write_b32 v10, v8 offset:24
	ds_write_b32 v10, v11 offset:56
	ds_write_b32 v10, v13 offset:88
	v_add_u32_e32 v12, 0xff, v8
	v_ashrrev_i32_e32 v12, 8, v12
	v_add_u32_e32 v11, v11, v12
	v_mul_u32_u24_e32 v13, 56, v11
	ds_write_b32 v10, v9 offset:28
	ds_write_b32 v10, v11 offset:60
	ds_write_b32 v10, v13 offset:92
	v_add_u32_e32 v12, 0xff, v9
	v_ashrrev_i32_e32 v12, 8, v12
	v_add_u32_e32 v11, v11, v12
	v_mul_u32_u24_e32 v13, 56, v11
	ds_write_b32 v10, v13 offset:96

; #define LAS __attribute__((address_space(3)))
; __device__ __forceinline__ int tid_opaque() { int t = threadIdx.x; asm volatile("" : "+v"(t)); return t; }
; #define MKCTX() const Ctx P{InTbl{in_tbl()}, (float*)*(__attribute__((address_space(1))) float* const*)((const char*)in_tbl() + offsetof(Params, out)), ws}
; #define IN(k) (((PH_MASK >> (k)) & 1) && KARG_I(ph_lo) <= (k) && (k) < KARG_I(ph_hi))
; __device__ __forceinline__ void moe_tables(const Ctx& P, volatile LAS int* tab, int nN) {
;     if (tid_opaque() == 0) { const unsigned* ecnt = (const unsigned*)(P.ws + WS_CTL) + CW_ECNT; int pb = 0, cu = 0;
;         for (int e = 0; e < 8; ++e) { const int c = (int)ecnt[64 * e], np = (c + 255) >> 8; tab[e] = c; tab[8 + e] = pb; tab[16 + e] = cu; pb += np; cu += np * nN; }
;         tab[24] = cu; }
;     __syncthreads();
; }
; __global__ void __launch_bounds__(512, 2) fwd_kernel(Params KP) {
;     ...
;     if (IN(15)) { MKCTX();
;         moe_tables(P, tab, 8);
.Lp15_reenter:
	s_mov_b64 s[2:3], s[0:1]
	s_nop 0
	v_mov_b64_e32 v[2:3], s[2:3]
	flat_load_dword v1, v[2:3] offset:296
	s_waitcnt vmcnt(0) lgkmcnt(0)
	v_cmp_gt_i32_e32 vcc, 16, v1
	s_and_saveexec_b64 s[10:11], vcc
	s_cbranch_execz .LBB0_2648
	s_mov_b64 s[2:3], s[0:1]
	s_nop 0
	v_mov_b64_e32 v[2:3], s[2:3]
	flat_load_dword v1, v[2:3] offset:300
	s_waitcnt vmcnt(0) lgkmcnt(0)
	v_cmp_lt_i32_e32 vcc, 15, v1
	s_and_b64 exec, exec, vcc
	s_cbranch_execz .LBB0_2648
	s_cmp_eq_u32 s99, 0
	s_cselect_b32 s99, 1, s99
	s_mov_b64 s[2:3], s[0:1]
	s_mov_b64 s[2:3], s[0:1]
	v_mov_b32_e32 v1, v0
	s_nop 0
	v_cmp_eq_u32_e32 vcc, 0, v1
	s_and_saveexec_b64 s[2:3], vcc
	s_cbranch_execz .LBB0_2619
	s_cmp_eq_u32 s99, 2
	s_cbranch_scc1 .Lp15_tabfix
	v_mov_b32_e32 v1, 0x4000
	global_load_dword v2, v1, s[36:37]
	global_load_dword v3, v1, s[36:37] offset:256
	global_load_dword v4, v1, s[36:37] offset:512
	global_load_dword v5, v1, s[36:37] offset:768
	global_load_dword v6, v1, s[36:37] offset:1024
	global_load_dword v7, v1, s[36:37] offset:1280
	global_load_dword v8, v1, s[36:37] offset:1536
	global_load_dword v9, v1, s[36:37] offset:1792
	v_mov_b32_e32 v10, 0x20100
	v_mov_b32_e32 v11, 0
	v_mov_b32_e32 v13, 0
	s_waitcnt vmcnt(0)
	ds_write_b32 v10, v2
	ds_write_b32 v10, v11 offset:32
	ds_write_b32 v10, v13 offset:64
	v_add_u32_e32 v12, 0xff, v2
	v_ashrrev_i32_e32 v12, 8, v12
	v_add_u32_e32 v11, v11, v12
	v_lshlrev_b32_e32 v13, 3, v11
	ds_write_b32 v10, v3 offset:4
	ds_write_b32 v10, v11 offset:36
	ds_write_b32 v10, v13 offset:68
	v_add_u32_e32 v12, 0xff, v3
	v_ashrrev_i32_e32 v12, 8, v12
	v_add_u32_e32 v11, v11, v12
	v_lshlrev_b32_e32 v13, 3, v11
	ds_write_b32 v10, v4 offset:8
	ds_write_b32 v10, v11 offset:40
	ds_write_b32 v10, v13 offset:72
	v_add_u32_e32 v12, 0xff, v4
	v_ashrrev_i32_e32 v12, 8, v12
	v_add_u32_e32 v11, v11, v12
	v_lshlrev_b32_e32 v13, 3, v11
	ds_write_b32 v10, v5 offset:12
	ds_write_b32 v10, v11 offset:44
	ds_write_b32 v10, v13 offset:76
	v_add_u32_e32 v12, 0xff, v5
	v_ashrrev_i32_e32 v12, 8, v12
	v_add_u32_e32 v11, v11, v12
	v_lshlrev_b32_e32 v13, 3, v11
	ds_write_b32 v10, v6 offset:16
	ds_write_b32 v10, v11 offset:48
	ds_write_b32 v10, v13 offset:80
	v_add_u32_e32 v12, 0xff, v6
	v_ashrrev_i32_e32 v12, 8, v12
	v_add_u32_e32 v11, v11, v12
	v_lshlrev_b32_e32 v13, 3, v11
	ds_write_b32 v10, v7 offset:20
	ds_write_b32 v10, v11 offset:52
	ds_write_b32 v10, v13 offset:84
	v_add_u32_e32 v12, 0xff, v7
	v_ashrrev_i32_e32 v12, 8, v12
	v_add_u32_e32 v11, v11, v12
	v_lshlrev_b32_e32 v13, 3, v11
	ds_write_b32 v10, v8 offset:24
	ds_write_b32 v10, v11 offset:56
	ds_write_b32 v10, v13 offset:88
	v_add_u32_e32 v12, 0xff, v8
	v_ashrrev_i32_e32 v12, 8, v12
	v_add_u32_e32 v11, v11, v12
	v_lshlrev_b32_e32 v13, 3, v11
	ds_write_b32 v10, v9 offset:28
	ds_write_b32 v10, v11 offset:60
	ds_write_b32 v10, v13 offset:92
	v_add_u32_e32 v12, 0xff, v9
	v_ashrrev_i32_e32 v12, 8, v12
	v_add_u32_e32 v11, v11, v12
	v_lshlrev_b32_e32 v13, 3, v11
	v_min_i32_e32 v14, s101, v13
	ds_write_b32 v10, v13 offset:112
	ds_write_b32 v10, v14 offset:96
	s_branch .LBB0_2619
